# v56 + grid barrier: waiting workgroups poll the top-level generation word directly (skips the per-XCD relay hop)
# speedup vs baseline: 1.0030x; 1.0030x over previous
; __device__ __forceinline__ unsigned xb_ld(unsigned* p)              { return __hip_atomic_load(p, __ATOMIC_RELAXED, __HIP_MEMORY_SCOPE_AGENT); }
; __device__ __forceinline__ unsigned xb_add(unsigned* p, unsigned v) { return __hip_atomic_fetch_add(p, v, __ATOMIC_RELAXED, __HIP_MEMORY_SCOPE_AGENT); }
; #define XB_SPIN(cond, bar) do { unsigned _sp = 0; while (cond) { __builtin_amdgcn_s_sleep(1); \
;     if ((++_sp & 255u) == 0u) { if (xb_ld(&(bar)[XB_TMO])) break; if (_sp > XB_SPIN_CAP) { atomicAdd(&(bar)[XB_TMO], 1u); break; } } } } while (0)
; __device__ __forceinline__ void xcd_barrier(const XcdBarrier& b) {
;     ...
;         const unsigned old = xb_add(&bar[XB_XSUB(b.x)], 1u);
;         const unsigned gen = old / nloc;
;         if (old + 1u == (gen + 1u) * nloc) {
;             __builtin_amdgcn_fence(__ATOMIC_RELEASE, "agent");
;             asm volatile("s_waitcnt vmcnt(0)" ::: "memory");
;             const unsigned og = xb_add(&bar[XB_TOP], 1u);
;             const unsigned tg = og / nx;
;             if (og + 1u == (tg + 1u) * nx) xb_add(&bar[XB_TOPGEN], 1u);
;             else XB_SPIN(xb_ld(&bar[XB_TOPGEN]) == tg, bar);
;             __builtin_amdgcn_fence(__ATOMIC_ACQUIRE, "agent");
;             xb_add(&bar[XB_XGEN(b.x)], 1u);
;             asm volatile("s_waitcnt vmcnt(0)" ::: "memory");
;         } else {
;             XB_SPIN(xb_ld(&bar[XB_XGEN(b.x)]) == gen, bar);
.LBB0_162:
	s_lshl_b32 s0, s54, 8
	s_add_u32 s25, s55, s0
	s_addc_u32 s24, s56, 0
	v_mov_b32_e32 v3, s25
	v_add_co_u32_e32 v6, vcc, 0x1000, v3
	v_mov_b32_e32 v3, s24
	s_nop 0
	v_addc_co_u32_e32 v7, vcc, 0, v3, vcc
	v_mov_b32_e32 v3, 1
	flat_atomic_add v3, v[6:7], v3 offset:1024 sc0
	v_cvt_f32_u32_e32 v5, v4
	v_sub_u32_e32 v6, 0, v4
	v_rcp_iflag_f32_e32 v5, v5
	s_nop 0
	v_mul_f32_e32 v5, 0x4f7ffffe, v5
	v_cvt_u32_f32_e32 v5, v5
	v_mul_lo_u32 v6, v6, v5
	v_mul_hi_u32 v6, v5, v6
	v_add_u32_e32 v5, v5, v6
	s_waitcnt vmcnt(0) lgkmcnt(0)
	v_mul_hi_u32 v5, v3, v5
	v_mul_lo_u32 v7, v5, v4
	v_add_u32_e32 v6, 1, v3
	v_sub_u32_e32 v3, v3, v7
	v_add_u32_e32 v8, 1, v5
	v_cmp_ge_u32_e32 vcc, v3, v4
	v_sub_u32_e32 v7, v3, v4
	s_nop 0
	v_cndmask_b32_e32 v5, v5, v8, vcc
	v_cndmask_b32_e32 v3, v3, v7, vcc
	v_add_u32_e32 v7, 1, v5
	v_cmp_ge_u32_e32 vcc, v3, v4
	s_nop 1
	v_cndmask_b32_e32 v3, v5, v7, vcc
	v_mad_u64_u32 v[4:5], s[0:1], v4, v3, v[4:5]
	v_cmp_ne_u32_e32 vcc, v6, v4
	s_and_saveexec_b64 s[0:1], vcc
	s_xor_b64 s[0:1], exec, s[0:1]
	s_cbranch_execz .LBB0_175
	v_mov_b32_e32 v2, s25
	v_add_co_u32_e32 v4, vcc, 0x2000, v2
	v_mov_b32_e32 v2, s24
	s_nop 0
	v_addc_co_u32_e32 v5, vcc, 0, v2, vcc
	s_add_u32 s8, s36, 0x7500
	s_addc_u32 s9, s37, 0
	v_mov_b64_e32 v[4:5], s[8:9]
	flat_load_dword v2, v[4:5] sc1
	s_waitcnt vmcnt(0) lgkmcnt(0)
	v_cmp_eq_u32_e32 vcc, v2, v3
	s_and_saveexec_b64 s[4:5], vcc
	s_cbranch_execz .LBB0_174
	s_add_u32 s6, s36, 0x4200
	s_addc_u32 s7, s37, 0
	s_mov_b32 s26, 1
	s_mov_b64 s[10:11], 0
	s_branch .LBB0_166
